# baseline (speedup 1.0000x reference)
_Z11proj_kernelPKcPKfS2_Pf:
	s_load_dwordx8 s[4:11], s[0:1], 0x0
	s_lshl_b32 s0, s2, 6
	s_and_b32 s0, s0, 0x1c0
	s_ashr_i32 s2, s2, 3
	s_add_i32 s0, s0, s2
	s_ashr_i32 s0, s0, 5
	s_and_b32 s26, s2, 3
	s_ashr_i32 s1, s0, 31
	s_lshl_b32 s2, s2, 5
	s_lshl_b32 s12, s26, 16
	s_and_b32 s27, s2, 0x380
	s_lshl_b64 s[2:3], s[0:1], 16
	s_waitcnt lgkmcnt(0)
	s_add_u32 s1, s4, s2
	s_addc_u32 s13, s5, s3
	s_add_u32 s2, s4, s12
	v_lshrrev_b32_e32 v1, 4, v0
	s_addc_u32 s3, s5, 0
	s_lshl_b32 s4, s27, 6
	v_xor_b32_e32 v4, v1, v0
	s_add_u32 s4, s1, s4
	v_lshlrev_b32_e32 v130, 9, v1
	v_lshlrev_b32_e32 v1, 4, v4
	s_addc_u32 s5, s13, 0
	v_mov_b32_e32 v131, 0
	v_and_b32_e32 v4, 0xf0, v1
	v_lshrrev_b32_e32 v1, 1, v0
	v_mov_b32_e32 v5, v131
	v_lshrrev_b32_e32 v192, 3, v130
	v_mov_b32_e32 v193, 0
	v_lshl_add_u64 v[6:7], s[4:5], 0, v[192:193]
	v_and_b32_e32 v136, 64, v1
	v_lshlrev_b32_e32 v1, 4, v0
	v_lshl_add_u64 v[2:3], s[2:3], 0, v[130:131]
	v_and_b32_e32 v194, 48, v4
	v_and_b32_e32 v195, 0xc0, v4
	v_lshl_add_u32 v194, v195, 14, v194
	v_mov_b32_e32 v195, 0
	v_lshl_add_u64 v[134:135], v[6:7], 0, v[194:195]
	v_add_u32_e32 v6, 0, v1
	v_lshl_add_u64 v[132:133], v[2:3], 0, v[4:5]
	s_mov_b64 s[2:3], 0x280000
	v_readfirstlane_b32 s5, v6
	v_lshl_add_u64 v[2:3], v[132:133], 0, s[2:3]
	s_mov_b32 m0, s5
	s_mov_b64 s[2:3], 0x4900000
	global_load_lds_dwordx4 v[2:3], off
	v_add_u32_e32 v2, 0x8000, v6
	v_lshl_add_u64 v[4:5], v[134:135], 0, s[2:3]
	v_readfirstlane_b32 s4, v2
	s_mov_b32 m0, s4
	s_mov_b64 s[2:3], 0x282000
	global_load_lds_dwordx4 v[4:5], off
	v_add_u32_e32 v4, 0x1000, v6
	v_lshl_add_u64 v[2:3], v[132:133], 0, s[2:3]
	v_readfirstlane_b32 s12, v4
	v_add_u32_e32 v4, 0x9000, v6
	s_mov_b32 m0, s12
	s_mov_b64 s[2:3], 0x4900400
	v_readfirstlane_b32 s13, v4
	v_add_u32_e32 v4, 0x2000, v6
	global_load_lds_dwordx4 v[2:3], off
	v_lshl_add_u64 v[2:3], v[134:135], 0, s[2:3]
	s_mov_b32 m0, s13
	s_mov_b64 s[2:3], 0x284000
	v_readfirstlane_b32 s14, v4
	v_add_u32_e32 v4, 0xa000, v6
	global_load_lds_dwordx4 v[2:3], off
	v_lshl_add_u64 v[2:3], v[132:133], 0, s[2:3]
	s_mov_b32 m0, s14
	s_mov_b64 s[2:3], 0x4900800
	v_readfirstlane_b32 s15, v4
	v_add_u32_e32 v4, 0x3000, v6
	global_load_lds_dwordx4 v[2:3], off
	v_lshl_add_u64 v[2:3], v[134:135], 0, s[2:3]
	s_mov_b32 m0, s15
	s_mov_b64 s[2:3], 0x286000
	v_readfirstlane_b32 s16, v4
	v_add_u32_e32 v4, 0xb000, v6
	global_load_lds_dwordx4 v[2:3], off
	v_lshl_add_u64 v[2:3], v[132:133], 0, s[2:3]
	s_mov_b32 m0, s16
	s_mov_b64 s[2:3], 0x4900c00
	v_readfirstlane_b32 s17, v4
	v_add_u32_e32 v4, 0x4000, v6
	global_load_lds_dwordx4 v[2:3], off
	v_lshl_add_u64 v[2:3], v[134:135], 0, s[2:3]
	s_mov_b32 m0, s17
	s_mov_b64 s[2:3], 0x288000
	v_readfirstlane_b32 s18, v4
	v_add_u32_e32 v4, 0xc000, v6
	global_load_lds_dwordx4 v[2:3], off
	v_lshl_add_u64 v[2:3], v[132:133], 0, s[2:3]
	s_mov_b32 m0, s18
	s_mov_b64 s[2:3], 0x4901000
	v_readfirstlane_b32 s19, v4
	v_add_u32_e32 v4, 0x5000, v6
	global_load_lds_dwordx4 v[2:3], off
	v_lshl_add_u64 v[2:3], v[134:135], 0, s[2:3]
	s_mov_b32 m0, s19
	s_mov_b64 s[2:3], 0x28a000
	v_readfirstlane_b32 s20, v4
	v_add_u32_e32 v4, 0xd000, v6
	global_load_lds_dwordx4 v[2:3], off
	v_lshl_add_u64 v[2:3], v[132:133], 0, s[2:3]
	s_mov_b32 m0, s20
	s_mov_b64 s[2:3], 0x4901400
	v_readfirstlane_b32 s21, v4
	v_add_u32_e32 v4, 0x6000, v6
	global_load_lds_dwordx4 v[2:3], off
	v_lshl_add_u64 v[2:3], v[134:135], 0, s[2:3]
	s_mov_b32 m0, s21
	s_mov_b64 s[2:3], 0x28c000
	v_readfirstlane_b32 s22, v4
	v_add_u32_e32 v4, 0xe000, v6
	global_load_lds_dwordx4 v[2:3], off
	v_lshl_add_u64 v[2:3], v[132:133], 0, s[2:3]
	s_mov_b32 m0, s22
	s_mov_b64 s[2:3], 0x4901800
	v_readfirstlane_b32 s23, v4
	v_add_u32_e32 v4, 0x7000, v6
	global_load_lds_dwordx4 v[2:3], off
	v_lshl_add_u64 v[2:3], v[134:135], 0, s[2:3]
	s_mov_b32 m0, s23
	s_mov_b64 s[2:3], 0x28e000
	v_readfirstlane_b32 s24, v4
	global_load_lds_dwordx4 v[2:3], off
	v_lshl_add_u64 v[2:3], v[132:133], 0, s[2:3]
	s_mov_b32 m0, s24
	s_mov_b64 s[2:3], 0x4901c00
	global_load_lds_dwordx4 v[2:3], off
	v_lshl_add_u64 v[2:3], v[134:135], 0, s[2:3]
	s_lshl_b32 s0, s0, 9
	s_lshl_b32 s2, s26, 7
	s_or_b32 s0, s0, s2
	s_ashr_i32 s1, s0, 31
	s_lshl_b64 s[0:1], s[0:1], 12
	s_lshl_b32 s3, s27, 2
	v_add_u32_e32 v4, 0xf000, v6
	s_or_b32 s3, s0, s3
	v_readfirstlane_b32 s25, v4
	s_add_u32 s6, s6, s3
	s_mov_b32 m0, s25
	s_addc_u32 s7, s7, s1
	v_and_b32_e32 v130, 0x1f0, v1
	v_lshlrev_b32_e32 v1, 7, v0
	global_load_lds_dwordx4 v[2:3], off
	v_lshlrev_b32_e32 v28, 5, v0
	v_lshl_add_u64 v[2:3], s[6:7], 0, v[130:131]
	v_and_b32_e32 v130, 0x7000, v1
	s_movk_i32 s0, 0x3c00
	v_mov_b32_e32 v1, 0x2000
	v_bitop3_b32 v1, v28, s0, v1 bitop3:0xc8
	v_lshl_add_u64 v[4:5], v[2:3], 0, v[130:131]
	v_lshlrev_b32_e32 v130, 2, v1
	s_movk_i32 s0, 0x5c00
	v_mov_b32_e32 v1, 0x4000
	v_bitop3_b32 v1, v28, s0, v1 bitop3:0xc8
	v_lshl_add_u64 v[6:7], v[2:3], 0, v[130:131]
	v_lshlrev_b32_e32 v130, 2, v1
	s_movk_i32 s0, 0x7c00
	v_mov_b32_e32 v1, 0x6000
	v_bitop3_b32 v1, v28, s0, v1 bitop3:0xc8
	v_lshl_add_u64 v[8:9], v[2:3], 0, v[130:131]
	v_lshlrev_b32_e32 v130, 2, v1
	s_mov_b32 s0, 0xbc00
	v_mov_b32_e32 v1, 0xa000
	v_bitop3_b32 v1, v28, s0, v1 bitop3:0xc8
	v_lshl_add_u64 v[10:11], v[2:3], 0, v[130:131]
	v_lshlrev_b32_e32 v130, 2, v1
	s_mov_b32 s0, 0xdc00
	v_mov_b32_e32 v1, 0xc000
	v_bitop3_b32 v1, v28, s0, v1 bitop3:0xc8
	v_lshl_add_u64 v[12:13], v[2:3], 0, v[130:131]
	v_lshlrev_b32_e32 v130, 2, v1
	s_mov_b32 s0, 0xfc00
	v_mov_b32_e32 v1, 0xe000
	v_bitop3_b32 v1, v28, s0, v1 bitop3:0xc8
	v_lshl_add_u64 v[14:15], v[2:3], 0, v[130:131]
	v_lshlrev_b32_e32 v130, 2, v1
	s_mov_b32 s0, 0x13c00
	v_mov_b32_e32 v1, 0x12000
	v_bitop3_b32 v1, v28, s0, v1 bitop3:0xc8
	v_lshl_add_u64 v[16:17], v[2:3], 0, v[130:131]
	v_lshlrev_b32_e32 v130, 2, v1
	s_mov_b32 s0, 0x15c00
	v_mov_b32_e32 v1, 0x14000
	v_bitop3_b32 v1, v28, s0, v1 bitop3:0xc8
	v_lshl_add_u64 v[18:19], v[2:3], 0, v[130:131]
	v_lshlrev_b32_e32 v130, 2, v1
	s_mov_b32 s0, 0x17c00
	v_mov_b32_e32 v1, 0x16000
	v_bitop3_b32 v1, v28, s0, v1 bitop3:0xc8
	v_lshl_add_u64 v[20:21], v[2:3], 0, v[130:131]
	v_lshlrev_b32_e32 v130, 2, v1
	s_mov_b32 s0, 0x1bc00
	v_mov_b32_e32 v1, 0x1a000
	v_bitop3_b32 v1, v28, s0, v1 bitop3:0xc8
	v_lshl_add_u64 v[22:23], v[2:3], 0, v[130:131]
	v_lshlrev_b32_e32 v130, 2, v1
	s_mov_b32 s0, 0x1dc00
	v_mov_b32_e32 v1, 0x1c000
	v_bitop3_b32 v1, v28, s0, v1 bitop3:0xc8
	v_lshl_add_u64 v[24:25], v[2:3], 0, v[130:131]
	v_lshlrev_b32_e32 v130, 2, v1
	s_mov_b32 s0, 0x1fc00
	v_mov_b32_e32 v1, 0x1e000
	v_bitop3_b32 v1, v28, s0, v1 bitop3:0xc8
	s_mov_b32 s0, 0x20000
	global_load_dwordx4 v[126:129], v[4:5], off nt
	global_load_dwordx4 v[122:125], v[6:7], off nt
	global_load_dwordx4 v[114:117], v[8:9], off nt
	global_load_dwordx4 v[110:113], v[10:11], off nt
	v_add_co_u32_e32 v6, vcc, s0, v4
	s_mov_b32 s0, 0x40000
	s_nop 0
	v_addc_co_u32_e32 v7, vcc, 0, v5, vcc
	v_add_co_u32_e32 v8, vcc, s0, v4
	s_mov_b32 s0, 0x60000
	s_nop 0
	v_addc_co_u32_e32 v9, vcc, 0, v5, vcc
	v_lshl_add_u64 v[26:27], v[2:3], 0, v[130:131]
	v_lshlrev_b32_e32 v130, 2, v1
	v_add_co_u32_e32 v4, vcc, s0, v4
	v_lshl_add_u64 v[2:3], v[2:3], 0, v[130:131]
	global_load_dwordx4 v[106:109], v[12:13], off nt
	global_load_dwordx4 v[102:105], v[14:15], off nt
	global_load_dwordx4 v[94:97], v[16:17], off nt
	global_load_dwordx4 v[90:93], v[18:19], off nt
	v_addc_co_u32_e32 v5, vcc, 0, v5, vcc
	global_load_dwordx4 v[86:89], v[20:21], off nt
	global_load_dwordx4 v[82:85], v[22:23], off nt
	global_load_dwordx4 v[98:101], v[8:9], off nt
	global_load_dwordx4 v[78:81], v[4:5], off nt
	global_load_dwordx4 v[74:77], v[24:25], off nt
	global_load_dwordx4 v[70:73], v[26:27], off nt
	global_load_dwordx4 v[118:121], v[6:7], off nt
	global_load_dwordx4 v[66:69], v[2:3], off nt
	v_and_b32_e32 v1, 31, v0
	v_or_b32_e32 v2, v136, v1
	v_lshl_add_u32 v137, v2, 8, 0
	v_lshlrev_b32_e32 v2, 8, v0
	v_bfe_u32 v130, v0, 5, 1
	v_and_b32_e32 v2, 0x5f00, v2
	v_lshlrev_b32_e32 v171, 1, v130
	v_add_u32_e32 v170, 0, v2
	v_bitop3_b32 v2, v171, v0, 15 bitop3:0x78
	v_and_b32_e32 v172, 15, v0
	v_lshlrev_b32_e32 v10, 4, v2
	v_bitop3_b32 v2, v171, v172, 1 bitop3:0x36
	v_lshlrev_b32_e32 v11, 4, v2
	s_waitcnt vmcnt(16) lgkmcnt(0)
	s_barrier
	v_add_u32_e32 v173, v137, v10
	v_add_u32_e32 v176, v170, v11
	v_add_u32_e32 v174, v137, v11
	ds_read_b128 v[2:5], v173
	ds_read_b128 v[6:9], v174
	ds_read_b128 v[14:17], v176 offset:32768
	v_add_u32_e32 v175, v170, v10
	ds_read_b128 v[10:13], v175 offset:32768
	ds_read_b128 v[18:21], v175 offset:40960
	ds_read_b128 v[22:25], v176 offset:40960
	ds_read_b128 v[26:29], v173 offset:8192
	ds_read_b128 v[30:33], v174 offset:8192
	v_bitop3_b32 v50, v171, v172, 4 bitop3:0x36
	v_bitop3_b32 v51, v171, v172, 5 bitop3:0x36
	v_lshlrev_b32_e32 v50, 4, v50
	v_lshlrev_b32_e32 v51, 4, v51
	s_waitcnt lgkmcnt(0)
	v_mfma_f32_32x32x64_f8f6f4 v[34:49], v[2:9], v[10:17], 0
	v_add_u32_e32 v177, v137, v50
	v_add_u32_e32 v178, v137, v51
	v_add_u32_e32 v179, v170, v50
	v_add_u32_e32 v180, v170, v51
	ds_read_b128 v[138:141], v177
	ds_read_b128 v[142:145], v178
	ds_read_b128 v[150:153], v180 offset:32768
	ds_read_b128 v[146:149], v179 offset:32768
	ds_read_b128 v[154:157], v179 offset:40960
	ds_read_b128 v[158:161], v180 offset:40960
	ds_read_b128 v[162:165], v177 offset:8192
	ds_read_b128 v[166:169], v178 offset:8192
	s_mov_b64 s[6:7], 0x280100
	s_mov_b32 m0, s5
	v_lshl_or_b32 v130, v130, 2, v136
	v_mul_u32_u24_e32 v130, 0x210, v130
	s_mov_b32 s0, 0x3a800000
	v_mfma_f32_32x32x64_f8f6f4 v[50:65], v[2:9], v[18:25], 0
	v_mfma_f32_32x32x64_f8f6f4 v[2:17], v[26:33], v[10:17], 0
	v_mfma_f32_32x32x64_f8f6f4 v[18:33], v[26:33], v[18:25], 0
	s_waitcnt lgkmcnt(0)
	v_mfma_f32_32x32x64_f8f6f4 v[34:49], v[138:145], v[146:153], v[34:49]
	v_mfma_f32_32x32x64_f8f6f4 v[50:65], v[138:145], v[154:161], v[50:65]
	v_bitop3_b32 v138, v171, v172, 8 bitop3:0x36
	v_mfma_f32_32x32x64_f8f6f4 v[2:17], v[162:169], v[146:153], v[2:17]
	v_lshlrev_b32_e32 v146, 4, v138
	v_bitop3_b32 v138, v171, v172, 9 bitop3:0x36
	v_lshlrev_b32_e32 v147, 4, v138
	v_add_u32_e32 v181, v137, v146
	v_add_u32_e32 v182, v137, v147
	ds_read_b128 v[138:141], v181
	ds_read_b128 v[142:145], v182
	v_add_u32_e32 v184, v170, v147
	v_add_u32_e32 v183, v170, v146
	v_mfma_f32_32x32x64_f8f6f4 v[18:33], v[162:169], v[154:161], v[18:33]
	ds_read_b128 v[150:153], v184 offset:32768
	ds_read_b128 v[146:149], v183 offset:32768
	ds_read_b128 v[154:157], v183 offset:40960
	ds_read_b128 v[158:161], v184 offset:40960
	ds_read_b128 v[162:165], v181 offset:8192
	ds_read_b128 v[166:169], v182 offset:8192
	s_waitcnt lgkmcnt(0)
	v_mfma_f32_32x32x64_f8f6f4 v[34:49], v[138:145], v[146:153], v[34:49]
	v_mfma_f32_32x32x64_f8f6f4 v[50:65], v[138:145], v[154:161], v[50:65]
	v_bitop3_b32 v138, v171, v172, 12 bitop3:0x36
	v_bitop3_b32 v139, v171, v172, 13 bitop3:0x36
	v_mfma_f32_32x32x64_f8f6f4 v[2:17], v[162:169], v[146:153], v[2:17]
	v_lshlrev_b32_e32 v146, 4, v138
	v_lshlrev_b32_e32 v147, 4, v139
	v_add_u32_e32 v171, v137, v146
	v_add_u32_e32 v137, v137, v147
	ds_read_b128 v[138:141], v171
	ds_read_b128 v[142:145], v137
	v_add_u32_e32 v172, v170, v146
	v_add_u32_e32 v170, v170, v147
	v_mfma_f32_32x32x64_f8f6f4 v[18:33], v[162:169], v[154:161], v[18:33]
	ds_read_b128 v[150:153], v170 offset:32768
	ds_read_b128 v[146:149], v172 offset:32768
	ds_read_b128 v[154:157], v172 offset:40960
	ds_read_b128 v[158:161], v170 offset:40960
	ds_read_b128 v[162:165], v171 offset:8192
	ds_read_b128 v[166:169], v137 offset:8192
	s_waitcnt lgkmcnt(0)
	s_barrier
	s_waitcnt lgkmcnt(0)
	v_mfma_f32_32x32x64_f8f6f4 v[34:49], v[138:145], v[146:153], v[34:49]
	v_mfma_f32_32x32x64_f8f6f4 v[50:65], v[138:145], v[154:161], v[50:65]
	v_lshl_add_u64 v[138:139], v[132:133], 0, s[6:7]
	s_mov_b64 s[6:7], 0x4d00000
	global_load_lds_dwordx4 v[138:139], off
	v_lshl_add_u64 v[138:139], v[134:135], 0, s[6:7]
	s_mov_b32 m0, s4
	s_mov_b64 s[4:5], 0x282100
	global_load_lds_dwordx4 v[138:139], off
	v_lshl_add_u64 v[138:139], v[132:133], 0, s[4:5]
	s_mov_b32 m0, s12
	s_mov_b64 s[4:5], 0x4d00400
	global_load_lds_dwordx4 v[138:139], off
	v_lshl_add_u64 v[138:139], v[134:135], 0, s[4:5]
	s_mov_b32 m0, s13
	s_mov_b64 s[4:5], 0x284100
	global_load_lds_dwordx4 v[138:139], off
	v_lshl_add_u64 v[138:139], v[132:133], 0, s[4:5]
	s_mov_b32 m0, s14
	s_mov_b64 s[4:5], 0x4d00800
	global_load_lds_dwordx4 v[138:139], off
	v_lshl_add_u64 v[138:139], v[134:135], 0, s[4:5]
	s_mov_b32 m0, s15
	s_mov_b64 s[4:5], 0x286100
	global_load_lds_dwordx4 v[138:139], off
	v_lshl_add_u64 v[138:139], v[132:133], 0, s[4:5]
	s_mov_b32 m0, s16
	s_mov_b64 s[4:5], 0x4d00c00
	global_load_lds_dwordx4 v[138:139], off
	v_lshl_add_u64 v[138:139], v[134:135], 0, s[4:5]
	s_mov_b32 m0, s17
	s_mov_b64 s[4:5], 0x288100
	global_load_lds_dwordx4 v[138:139], off
	v_lshl_add_u64 v[138:139], v[132:133], 0, s[4:5]
	s_mov_b32 m0, s18
	s_mov_b64 s[4:5], 0x4d01000
	global_load_lds_dwordx4 v[138:139], off
	v_lshl_add_u64 v[138:139], v[134:135], 0, s[4:5]
	s_mov_b32 m0, s19
	s_mov_b64 s[4:5], 0x28a100
	global_load_lds_dwordx4 v[138:139], off
	v_lshl_add_u64 v[138:139], v[132:133], 0, s[4:5]
	s_mov_b32 m0, s20
	s_mov_b64 s[4:5], 0x4d01400
	global_load_lds_dwordx4 v[138:139], off
	v_lshl_add_u64 v[138:139], v[134:135], 0, s[4:5]
	s_mov_b32 m0, s21
	s_mov_b64 s[4:5], 0x28c100
	v_mfma_f32_32x32x64_f8f6f4 v[2:17], v[162:169], v[146:153], v[2:17]
	global_load_lds_dwordx4 v[138:139], off
	v_lshl_add_u64 v[138:139], v[132:133], 0, s[4:5]
	s_mov_b32 m0, s22
	s_mov_b64 s[4:5], 0x4d01800
	global_load_lds_dwordx4 v[138:139], off
	v_lshl_add_u64 v[138:139], v[134:135], 0, s[4:5]
	s_mov_b32 m0, s23
	s_mov_b64 s[4:5], 0x28e100
	global_load_lds_dwordx4 v[138:139], off
	v_lshl_add_u64 v[132:133], v[132:133], 0, s[4:5]
	s_mov_b32 m0, s24
	s_mov_b64 s[4:5], 0x4d01c00
	v_mfma_f32_32x32x64_f8f6f4 v[18:33], v[162:169], v[154:161], v[18:33]
	global_load_lds_dwordx4 v[132:133], off
	v_lshl_add_u64 v[132:133], v[134:135], 0, s[4:5]
	s_mov_b32 m0, s25
	s_movk_i32 s4, 0x210
	global_load_lds_dwordx4 v[132:133], off
	s_waitcnt vmcnt(0) lgkmcnt(0)
	s_barrier
	ds_read_b128 v[142:145], v174
	ds_read_b128 v[138:141], v173
	ds_read_b128 v[150:153], v176 offset:32768
	ds_read_b128 v[146:149], v175 offset:32768
	ds_read_b128 v[154:157], v175 offset:40960
	ds_read_b128 v[158:161], v176 offset:40960
	ds_read_b128 v[162:165], v173 offset:8192
	ds_read_b128 v[166:169], v174 offset:8192
	s_waitcnt lgkmcnt(4)
	v_mfma_f32_32x32x64_f8f6f4 v[34:49], v[138:145], v[146:153], v[34:49]
	v_lshlrev_b32_e32 v132, 2, v0
	v_and_b32_e32 v132, 0x17c, v132
	v_add3_u32 v130, 0, v132, v130
	v_add_u32_e32 v132, 0x400, v130
	s_add_u32 s6, s10, s3
	s_addc_u32 s7, s11, s1
	s_waitcnt lgkmcnt(2)
	v_mfma_f32_32x32x64_f8f6f4 v[50:65], v[138:145], v[154:161], v[50:65]
	s_waitcnt lgkmcnt(0)
	v_mfma_f32_32x32x64_f8f6f4 v[2:17], v[162:169], v[146:153], v[2:17]
	v_mfma_f32_32x32x64_f8f6f4 v[18:33], v[162:169], v[154:161], v[18:33]
	ds_read_b128 v[142:145], v178
	ds_read_b128 v[138:141], v177
	ds_read_b128 v[150:153], v180 offset:32768
	ds_read_b128 v[146:149], v179 offset:32768
	ds_read_b128 v[154:157], v179 offset:40960
	ds_read_b128 v[158:161], v180 offset:40960
	ds_read_b128 v[162:165], v177 offset:8192
	ds_read_b128 v[166:169], v178 offset:8192
	s_waitcnt lgkmcnt(4)
	v_mfma_f32_32x32x64_f8f6f4 v[34:49], v[138:145], v[146:153], v[34:49]
	s_waitcnt lgkmcnt(2)
	v_mfma_f32_32x32x64_f8f6f4 v[50:65], v[138:145], v[154:161], v[50:65]
	s_waitcnt lgkmcnt(0)
	v_mfma_f32_32x32x64_f8f6f4 v[2:17], v[162:169], v[146:153], v[2:17]
	v_mfma_f32_32x32x64_f8f6f4 v[18:33], v[162:169], v[154:161], v[18:33]
	ds_read_b128 v[142:145], v182
	ds_read_b128 v[138:141], v181
	ds_read_b128 v[150:153], v184 offset:32768
	ds_read_b128 v[146:149], v183 offset:32768
	ds_read_b128 v[154:157], v183 offset:40960
	ds_read_b128 v[158:161], v184 offset:40960
	ds_read_b128 v[162:165], v181 offset:8192
	ds_read_b128 v[166:169], v182 offset:8192
	s_waitcnt lgkmcnt(4)
	v_mfma_f32_32x32x64_f8f6f4 v[34:49], v[138:145], v[146:153], v[34:49]
	s_waitcnt lgkmcnt(2)
	v_mfma_f32_32x32x64_f8f6f4 v[50:65], v[138:145], v[154:161], v[50:65]
	s_waitcnt lgkmcnt(0)
	v_mfma_f32_32x32x64_f8f6f4 v[2:17], v[162:169], v[146:153], v[2:17]
	v_mfma_f32_32x32x64_f8f6f4 v[18:33], v[162:169], v[154:161], v[18:33]
	ds_read_b128 v[142:145], v137
	ds_read_b128 v[138:141], v171
	ds_read_b128 v[150:153], v170 offset:32768
	ds_read_b128 v[146:149], v172 offset:32768
	ds_read_b128 v[154:157], v172 offset:40960
	ds_read_b128 v[158:161], v170 offset:40960
	ds_read_b128 v[162:165], v171 offset:8192
	ds_read_b128 v[166:169], v137 offset:8192
	s_waitcnt lgkmcnt(0)
	s_barrier
	v_mfma_f32_32x32x64_f8f6f4 v[34:49], v[138:145], v[146:153], v[34:49]
	v_mfma_f32_32x32x64_f8f6f4 v[50:65], v[138:145], v[154:161], v[50:65]
	s_nop 15
	s_nop 2
	ds_write2_b32 v132, v36, v52 offset0:8 offset1:40
	ds_write2_b32 v132, v37, v53 offset0:140 offset1:172
	v_mfma_f32_32x32x64_f8f6f4 v[2:17], v[162:169], v[146:153], v[2:17]
	v_add_u32_e32 v36, 0x1000, v130
	ds_write2_b32 v36, v38, v54 offset0:32 offset1:64
	ds_write2_b32 v36, v39, v55 offset0:164 offset1:196
	v_add_u32_e32 v36, 0x1400, v130
	ds_write2_b32 v36, v40, v56 offset0:40 offset1:72
	ds_write2_b32 v36, v41, v57 offset0:172 offset1:204
	v_add_u32_e32 v36, 0x2000, v130
	ds_write2_b32 v36, v42, v58 offset0:64 offset1:96
	ds_write2_b32 v36, v43, v59 offset0:196 offset1:228
	v_add_u32_e32 v36, 0x2400, v130
	ds_write2_b32 v36, v44, v60 offset0:72 offset1:104
	ds_write2_b32 v36, v45, v61 offset0:204 offset1:236
	v_add_u32_e32 v36, 0x3000, v130
	ds_write2_b32 v36, v46, v62 offset0:96 offset1:128
	v_add_u32_e32 v36, 0x3200, v130
	ds_write2_b32 v36, v47, v63 offset0:100 offset1:132
	v_add_u32_e32 v36, 0x3400, v130
	ds_write2_b32 v36, v48, v64 offset0:104 offset1:136
	v_add_u32_e32 v36, 0x3600, v130
	v_mfma_f32_32x32x64_f8f6f4 v[18:33], v[162:169], v[154:161], v[18:33]
	ds_write2_b32 v36, v49, v65 offset0:108 offset1:140
	ds_write2_b32 v130, v34, v50 offset1:32
	ds_write2_b32 v130, v35, v51 offset0:132 offset1:164
	v_add_u32_e32 v34, 0x4000, v130
	s_nop 15
	ds_write2_b32 v34, v2, v18 offset0:128 offset1:160
	v_add_u32_e32 v2, 0x4400, v130
	ds_write2_b32 v2, v3, v19 offset0:4 offset1:36
	ds_write2_b32 v2, v4, v20 offset0:136 offset1:168
	v_add_u32_e32 v2, 0x4800, v130
	ds_write2_b32 v2, v5, v21 offset0:12 offset1:44
	v_add_u32_e32 v2, 0x5000, v130
	ds_write2_b32 v2, v6, v22 offset0:160 offset1:192
	v_add_u32_e32 v2, 0x5400, v130
	ds_write2_b32 v2, v7, v23 offset0:36 offset1:68
	ds_write2_b32 v2, v8, v24 offset0:168 offset1:200
	v_add_u32_e32 v2, 0x5800, v130
	ds_write2_b32 v2, v9, v25 offset0:44 offset1:76
	v_add_u32_e32 v2, 0x6000, v130
	ds_write2_b32 v2, v10, v26 offset0:192 offset1:224
	v_add_u32_e32 v2, 0x6400, v130
	ds_write2_b32 v2, v11, v27 offset0:68 offset1:100
	ds_write2_b32 v2, v12, v28 offset0:200 offset1:232
	v_add_u32_e32 v2, 0x6800, v130
	ds_write2_b32 v2, v13, v29 offset0:76 offset1:108
	v_add_u32_e32 v2, 0x7200, v130
	ds_write2_b32 v2, v14, v30 offset0:96 offset1:128
	v_add_u32_e32 v2, 0x7400, v130
	ds_write2_b32 v2, v15, v31 offset0:100 offset1:132
	v_add_u32_e32 v2, 0x7600, v130
	ds_write2_b32 v2, v16, v32 offset0:104 offset1:136
	v_add_u32_e32 v2, 0x7800, v130
	v_lshrrev_b32_e32 v21, 5, v0
	ds_write2_b32 v2, v17, v33 offset0:108 offset1:140
	v_or_b32_e32 v2, s2, v21
	v_lshlrev_b32_e32 v3, 2, v2
	s_waitcnt lgkmcnt(0)
	s_barrier
	global_load_dword v2, v3, s[8:9]
	v_or_b32_e32 v4, 0x100, v0
	v_lshrrev_b32_e32 v23, 5, v4
	v_or_b32_e32 v4, s2, v23
	v_lshlrev_b32_e32 v4, 2, v4
	global_load_dword v20, v4, s[8:9]
	v_or_b32_e32 v4, 0x200, v0
	v_lshrrev_b32_e32 v25, 5, v4
	v_or_b32_e32 v4, s2, v25
	v_lshlrev_b32_e32 v4, 2, v4
	global_load_dword v22, v4, s[8:9]
	v_or_b32_e32 v4, 0x300, v0
	v_lshrrev_b32_e32 v27, 5, v4
	v_or_b32_e32 v4, s2, v27
	v_lshlrev_b32_e32 v4, 2, v4
	global_load_dword v24, v4, s[8:9]
	global_load_dword v26, v3, s[8:9] offset:128
	v_or_b32_e32 v12, 0x500, v0
	v_lshlrev_b32_e32 v130, 4, v1
	v_lshrrev_b32_e32 v31, 5, v12
	v_add_u32_e32 v1, 0, v130
	v_or_b32_e32 v12, s2, v31
	v_mad_u32_u24 v29, v21, s4, v1
	v_lshlrev_b32_e32 v12, 2, v12
	ds_read_b128 v[4:7], v29
	ds_read_b128 v[8:11], v29 offset:16896
	global_load_dword v28, v12, s[8:9]
	s_waitcnt lgkmcnt(1)
	v_pk_fma_f32 v[6:7], v[6:7], s[0:1], v[128:129] op_sel_hi:[1,0,1]
	v_pk_fma_f32 v[12:13], v[4:5], s[0:1], v[126:127] op_sel_hi:[1,0,1]
	global_load_dword v30, v3, s[8:9] offset:256
	global_load_dword v4, v3, s[8:9] offset:384
	s_waitcnt vmcnt(7)
	v_pk_add_f32 v[14:15], v[6:7], v[2:3] op_sel_hi:[1,0]
	v_pk_add_f32 v[12:13], v[12:13], v[2:3] op_sel_hi:[1,0]
	v_mad_u32_u24 v2, v23, s4, v1
	ds_read_b128 v[16:19], v2
	v_or_b32_e32 v2, 0x600, v0
	v_lshrrev_b32_e32 v5, 5, v2
	v_or_b32_e32 v2, s2, v5
	v_lshlrev_b32_e32 v2, 2, v2
	global_load_dword v32, v2, s[8:9]
	v_lshl_add_u64 v[2:3], s[6:7], 0, v[130:131]
	v_lshlrev_b32_e32 v130, 12, v21
	v_lshl_add_u64 v[6:7], v[2:3], 0, v[130:131]
	global_store_dwordx4 v[6:7], v[12:15], off nt
	s_waitcnt lgkmcnt(0)
	v_pk_fma_f32 v[6:7], v[18:19], s[0:1], v[124:125] op_sel_hi:[1,0,1]
	s_waitcnt vmcnt(8)
	v_pk_add_f32 v[14:15], v[6:7], v[20:21] op_sel_hi:[1,0]
	v_mad_u32_u24 v6, v25, s4, v1
	v_pk_fma_f32 v[12:13], v[16:17], s[0:1], v[122:123] op_sel_hi:[1,0,1]
	ds_read_b128 v[16:19], v6
	v_lshlrev_b32_e32 v6, 12, v23
	v_mov_b32_e32 v7, v131
	v_pk_add_f32 v[12:13], v[12:13], v[20:21] op_sel_hi:[1,0]
	v_lshl_add_u64 v[6:7], v[2:3], 0, v[6:7]
	global_store_dwordx4 v[6:7], v[12:15], off nt
	s_waitcnt lgkmcnt(0)
	v_pk_fma_f32 v[6:7], v[18:19], s[0:1], v[116:117] op_sel_hi:[1,0,1]
	v_or_b32_e32 v12, 0x700, v0
	v_lshrrev_b32_e32 v21, 5, v12
	v_or_b32_e32 v12, s2, v21
	v_lshlrev_b32_e32 v12, 2, v12
	s_waitcnt vmcnt(8)
	v_pk_add_f32 v[14:15], v[6:7], v[22:23] op_sel_hi:[1,0]
	v_mad_u32_u24 v6, v27, s4, v1
	global_load_dword v20, v12, s[8:9]
	v_pk_fma_f32 v[12:13], v[16:17], s[0:1], v[114:115] op_sel_hi:[1,0,1]
	ds_read_b128 v[16:19], v6
	v_lshlrev_b32_e32 v6, 12, v25
	v_mov_b32_e32 v7, v131
	v_pk_add_f32 v[12:13], v[12:13], v[22:23] op_sel_hi:[1,0]
	v_lshl_add_u64 v[6:7], v[2:3], 0, v[6:7]
	global_store_dwordx4 v[6:7], v[12:15], off nt
	s_waitcnt lgkmcnt(0)
	v_pk_fma_f32 v[6:7], v[18:19], s[0:1], v[112:113] op_sel_hi:[1,0,1]
	v_pk_fma_f32 v[12:13], v[16:17], s[0:1], v[110:111] op_sel_hi:[1,0,1]
	v_or_b32_e32 v16, 0x900, v0
	v_lshrrev_b32_e32 v19, 5, v16
	v_or_b32_e32 v16, s2, v19
	s_waitcnt vmcnt(9)
	v_pk_add_f32 v[14:15], v[6:7], v[24:25] op_sel_hi:[1,0]
	v_lshlrev_b32_e32 v6, 12, v27
	v_mov_b32_e32 v7, v131
	v_lshlrev_b32_e32 v16, 2, v16
	v_pk_add_f32 v[12:13], v[12:13], v[24:25] op_sel_hi:[1,0]
	global_load_dword v18, v16, s[8:9]
	v_lshl_add_u64 v[6:7], v[2:3], 0, v[6:7]
	global_store_dwordx4 v[6:7], v[12:15], off nt
	v_pk_fma_f32 v[6:7], v[10:11], s[0:1], v[120:121] op_sel_hi:[1,0,1]
	v_pk_fma_f32 v[10:11], v[8:9], s[0:1], v[118:119] op_sel_hi:[1,0,1]
	s_waitcnt vmcnt(10)
	v_pk_add_f32 v[8:9], v[6:7], v[26:27] op_sel_hi:[1,0]
	v_or_b32_e32 v6, 0xa00, v0
	v_lshrrev_b32_e32 v23, 5, v6
	v_or_b32_e32 v6, s2, v23
	v_lshlrev_b32_e32 v6, 2, v6
	global_load_dword v22, v6, s[8:9]
	v_pk_add_f32 v[6:7], v[10:11], v[26:27] op_sel_hi:[1,0]
	v_mad_u32_u24 v10, v31, s4, v1
	v_or_b32_e32 v16, 0xb00, v0
	ds_read_b128 v[10:13], v10
	v_lshrrev_b32_e32 v25, 5, v16
	v_or_b32_e32 v16, s2, v25
	v_lshlrev_b32_e32 v16, 2, v16
	v_or_b32_e32 v14, 0x20000, v130
	v_mov_b32_e32 v15, v131
	global_load_dword v24, v16, s[8:9]
	v_lshl_add_u64 v[14:15], v[2:3], 0, v[14:15]
	global_store_dwordx4 v[14:15], v[6:9], off nt
	s_waitcnt lgkmcnt(0)
	v_pk_fma_f32 v[10:11], v[10:11], s[0:1], v[106:107] op_sel_hi:[1,0,1]
	v_lshlrev_b32_e32 v14, 12, v5
	v_pk_fma_f32 v[6:7], v[12:13], s[0:1], v[108:109] op_sel_hi:[1,0,1]
	v_mov_b32_e32 v15, v131
	s_waitcnt vmcnt(12)
	v_pk_add_f32 v[8:9], v[6:7], v[28:29] op_sel_hi:[1,0]
	v_pk_add_f32 v[6:7], v[10:11], v[28:29] op_sel_hi:[1,0]
	v_lshlrev_b32_e32 v10, 12, v31
	v_mov_b32_e32 v11, v131
	v_lshl_add_u64 v[10:11], v[2:3], 0, v[10:11]
	global_store_dwordx4 v[10:11], v[6:9], off nt
	v_or_b32_e32 v10, 0xd00, v0
	v_lshrrev_b32_e32 v27, 5, v10
	v_or_b32_e32 v10, s2, v27
	v_lshlrev_b32_e32 v10, 2, v10
	global_load_dword v26, v10, s[8:9]
	v_mad_u32_u24 v6, v5, s4, v1
	ds_read_b128 v[6:9], v6
	v_or_b32_e32 v10, 0xe00, v0
	v_lshrrev_b32_e32 v31, 5, v10
	v_or_b32_e32 v10, s2, v31
	v_lshlrev_b32_e32 v10, 2, v10
	global_load_dword v28, v10, s[8:9]
	v_mad_u32_u24 v10, v21, s4, v1
	ds_read_b128 v[10:13], v10
	s_waitcnt lgkmcnt(1)
	v_pk_fma_f32 v[8:9], v[8:9], s[0:1], v[104:105] op_sel_hi:[1,0,1]
	v_pk_fma_f32 v[6:7], v[6:7], s[0:1], v[102:103] op_sel_hi:[1,0,1]
	v_or_b32_e32 v0, 0xf00, v0
	s_waitcnt vmcnt(12)
	v_pk_add_f32 v[8:9], v[8:9], v[32:33] op_sel_hi:[1,0]
	v_pk_add_f32 v[6:7], v[6:7], v[32:33] op_sel_hi:[1,0]
	v_lshrrev_b32_e32 v32, 5, v0
	v_or_b32_e32 v0, s2, v32
	v_lshlrev_b32_e32 v0, 2, v0
	global_load_dword v0, v0, s[8:9]
	v_lshl_add_u64 v[14:15], v[2:3], 0, v[14:15]
	global_store_dwordx4 v[14:15], v[6:9], off nt
	s_waitcnt lgkmcnt(0)
	v_pk_fma_f32 v[10:11], v[10:11], s[0:1], v[94:95] op_sel_hi:[1,0,1]
	v_lshlrev_b32_e32 v14, 12, v21
	v_pk_fma_f32 v[6:7], v[12:13], s[0:1], v[96:97] op_sel_hi:[1,0,1]
	v_mov_b32_e32 v15, v131
	s_waitcnt vmcnt(11)
	v_pk_add_f32 v[8:9], v[6:7], v[20:21] op_sel_hi:[1,0]
	v_pk_add_f32 v[6:7], v[10:11], v[20:21] op_sel_hi:[1,0]
	ds_read_b128 v[10:13], v29 offset:33792
	v_lshl_add_u64 v[14:15], v[2:3], 0, v[14:15]
	v_mad_u32_u24 v5, v19, s4, v1
	global_store_dwordx4 v[14:15], v[6:9], off nt
	ds_read_b128 v[14:17], v5
	s_waitcnt lgkmcnt(1)
	v_pk_fma_f32 v[12:13], v[12:13], s[0:1], v[100:101] op_sel_hi:[1,0,1]
	v_pk_fma_f32 v[10:11], v[10:11], s[0:1], v[98:99] op_sel_hi:[1,0,1]
	v_or_b32_e32 v20, 0x40000, v130
	v_mov_b32_e32 v21, v131
	v_pk_add_f32 v[12:13], v[12:13], v[30:31] op_sel_hi:[1,0]
	v_pk_add_f32 v[10:11], v[10:11], v[30:31] op_sel_hi:[1,0]
	v_lshl_add_u64 v[20:21], v[2:3], 0, v[20:21]
	global_store_dwordx4 v[20:21], v[10:13], off nt
	s_waitcnt lgkmcnt(0)
	v_pk_fma_f32 v[14:15], v[14:15], s[0:1], v[90:91] op_sel_hi:[1,0,1]
	v_mad_u32_u24 v5, v23, s4, v1
	v_pk_fma_f32 v[10:11], v[16:17], s[0:1], v[92:93] op_sel_hi:[1,0,1]
	ds_read_b128 v[6:9], v29 offset:50688
	s_waitcnt vmcnt(11)
	v_pk_add_f32 v[12:13], v[10:11], v[18:19] op_sel_hi:[1,0]
	v_pk_add_f32 v[10:11], v[14:15], v[18:19] op_sel_hi:[1,0]
	ds_read_b128 v[14:17], v5
	v_lshlrev_b32_e32 v18, 12, v19
	v_mov_b32_e32 v19, v131
	v_lshl_add_u64 v[18:19], v[2:3], 0, v[18:19]
	global_store_dwordx4 v[18:19], v[10:13], off nt
	s_waitcnt lgkmcnt(0)
	v_pk_fma_f32 v[14:15], v[14:15], s[0:1], v[86:87] op_sel_hi:[1,0,1]
	v_mad_u32_u24 v5, v25, s4, v1
	v_pk_fma_f32 v[10:11], v[16:17], s[0:1], v[88:89] op_sel_hi:[1,0,1]
	v_lshlrev_b32_e32 v18, 12, v23
	s_waitcnt vmcnt(10)
	v_pk_add_f32 v[12:13], v[10:11], v[22:23] op_sel_hi:[1,0]
	v_pk_add_f32 v[10:11], v[14:15], v[22:23] op_sel_hi:[1,0]
	ds_read_b128 v[14:17], v5
	v_mov_b32_e32 v19, v131
	v_lshl_add_u64 v[18:19], v[2:3], 0, v[18:19]
	global_store_dwordx4 v[18:19], v[10:13], off nt
	v_pk_fma_f32 v[8:9], v[8:9], s[0:1], v[80:81] op_sel_hi:[1,0,1]
	s_waitcnt lgkmcnt(0)
	v_pk_fma_f32 v[14:15], v[14:15], s[0:1], v[82:83] op_sel_hi:[1,0,1]
	v_pk_fma_f32 v[10:11], v[16:17], s[0:1], v[84:85] op_sel_hi:[1,0,1]
	v_or_b32_e32 v130, 0x60000, v130
	s_waitcnt vmcnt(10)
	v_pk_add_f32 v[12:13], v[10:11], v[24:25] op_sel_hi:[1,0]
	v_pk_add_f32 v[10:11], v[14:15], v[24:25] op_sel_hi:[1,0]
	v_lshlrev_b32_e32 v14, 12, v25
	v_mov_b32_e32 v15, v131
	v_lshl_add_u64 v[14:15], v[2:3], 0, v[14:15]
	global_store_dwordx4 v[14:15], v[10:13], off nt
	s_nop 1
	v_pk_fma_f32 v[12:13], v[6:7], s[0:1], v[78:79] op_sel_hi:[1,0,1]
	v_pk_add_f32 v[6:7], v[8:9], v[4:5] op_sel_hi:[1,0]
	v_mad_u32_u24 v5, v27, s4, v1
	ds_read_b128 v[8:11], v5
	v_pk_add_f32 v[4:5], v[12:13], v[4:5] op_sel_hi:[1,0]
	v_lshl_add_u64 v[12:13], v[2:3], 0, v[130:131]
	global_store_dwordx4 v[12:13], v[4:7], off nt
	v_lshlrev_b32_e32 v130, 12, v27
	s_waitcnt lgkmcnt(0)
	v_pk_fma_f32 v[12:13], v[8:9], s[0:1], v[74:75] op_sel_hi:[1,0,1]
	v_pk_fma_f32 v[4:5], v[10:11], s[0:1], v[76:77] op_sel_hi:[1,0,1]
	s_waitcnt vmcnt(9)
	v_pk_add_f32 v[6:7], v[4:5], v[26:27] op_sel_hi:[1,0]
	v_mad_u32_u24 v4, v31, s4, v1
	ds_read_b128 v[8:11], v4
	v_pk_add_f32 v[4:5], v[12:13], v[26:27] op_sel_hi:[1,0]
	v_lshl_add_u64 v[12:13], v[2:3], 0, v[130:131]
	v_mad_u32_u24 v1, v32, s4, v1
	global_store_dwordx4 v[12:13], v[4:7], off nt
	s_waitcnt lgkmcnt(0)
	v_pk_fma_f32 v[12:13], v[8:9], s[0:1], v[70:71] op_sel_hi:[1,0,1]
	v_lshlrev_b32_e32 v130, 12, v31
	v_pk_fma_f32 v[4:5], v[10:11], s[0:1], v[72:73] op_sel_hi:[1,0,1]
	ds_read_b128 v[8:11], v1
	s_waitcnt vmcnt(9)
	v_pk_add_f32 v[6:7], v[4:5], v[28:29] op_sel_hi:[1,0]
	v_pk_add_f32 v[4:5], v[12:13], v[28:29] op_sel_hi:[1,0]
	v_lshl_add_u64 v[12:13], v[2:3], 0, v[130:131]
	global_store_dwordx4 v[12:13], v[4:7], off nt
	s_waitcnt lgkmcnt(0)
	v_pk_fma_f32 v[8:9], v[8:9], s[0:1], v[66:67] op_sel_hi:[1,0,1]
	v_lshlrev_b32_e32 v130, 12, v32
	v_pk_fma_f32 v[4:5], v[10:11], s[0:1], v[68:69] op_sel_hi:[1,0,1]
	s_waitcnt vmcnt(9)
	v_pk_add_f32 v[6:7], v[4:5], v[0:1] op_sel_hi:[1,0]
	v_pk_add_f32 v[4:5], v[8:9], v[0:1] op_sel_hi:[1,0]
	v_lshl_add_u64 v[0:1], v[2:3], 0, v[130:131]
	global_store_dwordx4 v[0:1], v[4:7], off nt
	s_endpgm

	.amdhsa_kernel _Z11proj_kernelPKcPKfS2_Pf
		.amdhsa_group_segment_fixed_size 0
		.amdhsa_private_segment_fixed_size 0
		.amdhsa_kernarg_size 32
		.amdhsa_user_sgpr_count 2
		.amdhsa_user_sgpr_dispatch_ptr 0
		.amdhsa_user_sgpr_queue_ptr 0
		.amdhsa_user_sgpr_kernarg_segment_ptr 1
		.amdhsa_user_sgpr_dispatch_id 0
		.amdhsa_user_sgpr_kernarg_preload_length 0
		.amdhsa_user_sgpr_kernarg_preload_offset 0
		.amdhsa_user_sgpr_private_segment_size 0
		.amdhsa_uses_dynamic_stack 0
		.amdhsa_enable_private_segment 0
		.amdhsa_system_sgpr_workgroup_id_x 1
		.amdhsa_system_sgpr_workgroup_id_y 0
		.amdhsa_system_sgpr_workgroup_id_z 0
		.amdhsa_system_sgpr_workgroup_info 0
		.amdhsa_system_vgpr_workitem_id 0
		.amdhsa_next_free_vgpr 196
		.amdhsa_next_free_sgpr 28
		.amdhsa_accum_offset 196
		.amdhsa_reserve_vcc 1
		.amdhsa_float_round_mode_32 0
		.amdhsa_float_round_mode_16_64 0
		.amdhsa_float_denorm_mode_32 3
		.amdhsa_float_denorm_mode_16_64 3
		.amdhsa_dx10_clamp 1
		.amdhsa_ieee_mode 1
		.amdhsa_fp16_overflow 0
		.amdhsa_tg_split 0
		.amdhsa_exception_fp_ieee_invalid_op 0
		.amdhsa_exception_fp_denorm_src 0
		.amdhsa_exception_fp_ieee_div_zero 0
		.amdhsa_exception_fp_ieee_overflow 0
		.amdhsa_exception_fp_ieee_underflow 0
		.amdhsa_exception_fp_ieee_inexact 0
		.amdhsa_exception_int_div_zero 0
	.end_amdhsa_kernel

_Z13attn11_kernelILi4EEvPc:
	s_ashr_i32 s5, s2, 3
	s_load_dwordx2 s[12:13], s[0:1], 0x0
	s_lshr_b32 s4, s5, 29
	s_lshl_b32 s3, s2, 4
	s_add_i32 s6, s5, s4
	s_and_b32 s3, s3, 0x70
	s_ashr_i32 s4, s6, 3
	s_add_i32 s4, s3, s4
	s_and_b32 s3, s6, 0x1fffff8
	s_sub_i32 s3, s5, s3
	v_lshrrev_b32_e32 v1, 6, v0
	s_waitcnt lgkmcnt(0)
	s_add_u32 s14, s12, 0x2500000
	v_lshlrev_b32_e32 v192, 5, v1
	s_addc_u32 s15, s13, 0
	s_ashr_i32 s5, s4, 31
	s_mul_i32 s6, s4, 0x12000
	v_lshl_or_b32 v172, s3, 7, v192
	s_mul_hi_i32 s3, s4, 0x12000
	s_add_u32 s8, s14, s6
	s_addc_u32 s9, s15, s3
	s_add_u32 s16, s12, 0x3700000
	v_lshlrev_b32_e32 v169, 4, v0
	s_addc_u32 s17, s13, 0
	s_add_u32 s10, s16, s6
	v_add_u32_e32 v193, 0, v169
	v_lshrrev_b32_e32 v2, 2, v0
	v_bitop3_b32 v3, v169, 48, v0 bitop3:0x48
	s_addc_u32 s11, s17, s3
	s_mov_b64 s[46:47], s[8:9]
	s_mov_b64 s[48:49], s[10:11]
	s_mov_b64 s[50:51], s[14:15]
	s_mov_b64 s[52:53], s[16:17]
	v_readfirstlane_b32 s3, v193
	v_add_u32_e32 v4, 0x8000, v193
	v_lshl_or_b32 v170, v2, 6, v3
	v_mul_u32_u24_e32 v2, 0x480, v2
	v_mov_b32_e32 v171, 0
	s_mov_b32 m0, s3
	v_readfirstlane_b32 s3, v4
	v_add_u32_e32 v6, 0x2000, v193
	v_or_b32_e32 v2, v2, v3
	v_lshl_add_u64 v[174:175], s[8:9], 0, v[170:171]
	v_mov_b32_e32 v3, v171
	global_load_lds_dwordx4 v170, s[8:9]
	v_mov_b32_e32 v220, v170
	s_mov_b32 m0, s3
	s_mov_b64 s[8:9], 0x1000
	v_readfirstlane_b32 s6, v6
	v_add_u32_e32 v6, 0x4000, v193
	v_lshl_add_u64 v[176:177], s[10:11], 0, v[2:3]
	global_load_lds_dwordx4 v2, s[10:11]
	v_mov_b32_e32 v221, v2
	v_lshl_add_u64 v[4:5], v[174:175], 0, s[8:9]
	s_mov_b32 m0, s6
	s_mov_b64 s[10:11], 0x2000
	v_readfirstlane_b32 s6, v6
	v_add_u32_e32 v6, 0xa000, v193
	global_load_lds_dwordx4 v[4:5], off
	v_lshl_add_u64 v[4:5], v[174:175], 0, s[10:11]
	s_mov_b32 m0, s6
	v_readfirstlane_b32 s6, v6
	s_add_u32 s18, s12, 0x1500000
	global_load_lds_dwordx4 v[4:5], off
	v_lshl_add_u64 v[4:5], v[176:177], 0, 64
	s_mov_b32 m0, s6
	s_addc_u32 s19, s13, 0
	s_lshl_b64 s[20:21], s[4:5], 10
	v_ashrrev_i32_e32 v173, 31, v172
	v_and_b32_e32 v168, 31, v0
	global_load_lds_dwordx4 v[4:5], off
	v_lshl_add_u64 v[4:5], s[20:21], 0, v[172:173]
	v_or_b32_e32 v4, v4, v168
	v_lshlrev_b64 v[4:5], 6, v[4:5]
	v_lshl_add_u64 v[4:5], s[18:19], 0, v[4:5]
	v_and_b32_e32 v6, 32, v0
	v_mov_b32_e32 v7, v171
	v_lshl_add_u64 v[4:5], v[4:5], 0, v[6:7]
	global_load_dwordx4 v[152:155], v[4:5], off
	global_load_dwordx4 v[156:159], v[4:5], off offset:16
	v_and_b32_e32 v4, 60, v0
	v_lshlrev_b32_e32 v5, 2, v0
	s_add_u32 s0, s0, 8
	s_movk_i32 s5, 0xa00
	v_lshlrev_b32_e32 v184, 4, v4
	v_or_b32_e32 v4, 64, v4
	v_bitop3_b32 v195, v5, v6, 48 bitop3:0x6c
	v_lshl_add_u64 v[178:179], s[14:15], 0, v[170:171]
	v_lshl_add_u64 v[180:181], s[16:17], 0, v[2:3]
	s_addc_u32 s1, s1, 0
	v_mad_u32_u24 v1, v1, s5, 0
	v_lshrrev_b32_e32 v2, 3, v0
	s_movk_i32 s5, 0x50
	v_and_b32_e32 v170, 48, v169
	v_bfe_u32 v0, v0, 2, 4
	v_lshrrev_b32_e32 v5, 2, v4
	v_mov_b32_e32 v144, 0x38383838
	v_bfe_u32 v226, v169, 6, 1
	v_bfe_u32 v227, v169, 8, 1
	v_cmp_eq_u32_e32 vcc, v226, v227
	s_nop 1
	v_cndmask_b32_e32 v144, 0, v144, vcc
	v_lshl_add_u64 v[182:183], s[18:19], 0, v[6:7]
	v_and_b32_e32 v2, 4, v2
	v_mad_u32_u24 v3, v168, s5, v1
	s_add_u32 s12, s12, 0x4900000
	v_add_u32_e32 v1, v1, v170
	v_mul_u32_u24_e32 v0, 0x50, v0
	v_mul_u32_u24_e32 v5, 0x50, v5
	s_movk_i32 s18, 0xffc0
	v_lshlrev_b32_e32 v199, 6, v168
	s_mov_b32 s7, 0
	s_movk_i32 s3, 0x2000
	s_movk_i32 s33, 0x4000
	v_mov_b32_e32 v173, 0x74747474
	v_mov_b32_e32 v194, 0x7f7f7f7f
	v_mov_b32_e32 v145, v144
	v_mov_b32_e32 v146, v144
	v_mov_b32_e32 v147, v144
	v_mov_b32_e32 v148, v144
	v_mov_b32_e32 v149, v144
	v_mov_b32_e32 v150, v144
	v_mov_b32_e32 v151, v144
	s_addc_u32 s13, s13, 0
	v_mov_b32_e32 v185, v171
	v_lshlrev_b32_e32 v186, 4, v4
	v_mov_b32_e32 v187, v171
	s_mov_b64 s[30:31], -1
	s_mov_b64 s[14:15], 0x3000
	s_mov_b64 s[16:17], 0xc0
	s_mov_b32 s19, -1
	s_mov_b32 s5, 0xff61b1e6
	s_mov_b32 s36, 0x41000000
	s_mov_b64 s[20:21], 0x80
	s_mov_b64 s[22:23], 0x11000
	s_mov_b64 s[24:25], 0x400
	s_mov_b64 s[26:27], 0x440
	s_mov_b32 s37, 0x42800000
	v_add_u32_e32 v196, v3, v2
	v_add_u32_e32 v197, v1, v0
	v_add_u32_e32 v198, v1, v5
	v_add_u32_e32 v197, 0x10000, v197
	v_add_u32_e32 v198, 0x10000, v198
	v_mov_b32_e32 v0, v171
	v_mov_b32_e32 v1, v171
	v_mov_b32_e32 v2, v171
	v_mov_b32_e32 v3, v171
	v_mov_b32_e32 v4, v171
	v_mov_b32_e32 v5, v171
	v_mov_b32_e32 v6, v171
	v_mov_b32_e32 v8, v171
	v_mov_b32_e32 v9, v171
	v_mov_b32_e32 v10, v171
	v_mov_b32_e32 v11, v171
	v_mov_b32_e32 v12, v171
	v_mov_b32_e32 v13, v171
	v_mov_b32_e32 v14, v171
	v_mov_b32_e32 v15, v171
	s_mov_b32 s38, 0
	v_mov_b32_e32 v160, v171
	v_mov_b32_e32 v161, v171
	v_mov_b32_e32 v162, v171
	v_mov_b32_e32 v163, v171
	v_mov_b32_e32 v164, v171
	v_mov_b32_e32 v165, v171
	v_mov_b32_e32 v166, v171
	v_mov_b32_e32 v167, v171
	v_xor_b32_e32 v200, 16, v195
	v_add_u32_e32 v201, 0, v199
	v_add_u32_e32 v222, v199, v195
	v_add_u32_e32 v223, v199, v200
	v_readfirstlane_b32 s40, v169
	v_add_u32_e32 v224, 0x8000, v222
	v_add_u32_e32 v225, 0x8000, v223
	v_add_u32_e32 v228, 0x1000, v220
	v_add_u32_e32 v229, 64, v221
	s_add_u32 s60, s40, 0x0
	s_add_u32 s61, s40, 0x2000
	s_add_u32 s62, s40, 0x4000
	s_add_u32 s63, s40, 0x6000
	s_add_u32 s64, s40, 0x8000
	s_add_u32 s65, s40, 0xa000
	s_add_u32 s66, s40, 0xc000
	s_add_u32 s67, s40, 0xe000
	v_mov_b32_e32 v202, 0x12000
	s_branch .LBB3_3

.LBB3_2:
	v_exp_f32_e32 v81, v112
	v_exp_f32_e32 v82, v113
	v_exp_f32_e32 v85, v116
	v_exp_f32_e32 v86, v117
	v_exp_f32_e32 v89, v120
	v_exp_f32_e32 v90, v121
	v_exp_f32_e32 v93, v124
	v_exp_f32_e32 v94, v125
	v_exp_f32_e32 v64, v64
	v_exp_f32_e32 v65, v65
	v_exp_f32_e32 v68, v68
	v_exp_f32_e32 v69, v69
	v_exp_f32_e32 v72, v72
	v_exp_f32_e32 v73, v73
	v_exp_f32_e32 v76, v76
	v_exp_f32_e32 v77, v77
	v_exp_f32_e32 v83, v114
	v_exp_f32_e32 v84, v115
	v_exp_f32_e32 v87, v118
	v_exp_f32_e32 v88, v119
	v_exp_f32_e32 v91, v122
	v_exp_f32_e32 v92, v123
	v_exp_f32_e32 v95, v126
	v_exp_f32_e32 v96, v127
	v_exp_f32_e32 v66, v66
	v_exp_f32_e32 v67, v67
	v_exp_f32_e32 v70, v70
	v_exp_f32_e32 v71, v71
	v_exp_f32_e32 v74, v74
	v_exp_f32_e32 v75, v75
	v_exp_f32_e32 v78, v78
	v_exp_f32_e32 v79, v79
	v_cvt_pk_fp8_f32 v160, v81, v82
	v_cvt_pk_fp8_f32 v161, v85, v86
	v_cvt_pk_fp8_f32 v162, v89, v90
	v_cvt_pk_fp8_f32 v163, v93, v94
	v_cvt_pk_fp8_f32 v164, v64, v65
	v_cvt_pk_fp8_f32 v165, v68, v69
	v_cvt_pk_fp8_f32 v166, v72, v73
	v_cvt_pk_fp8_f32 v167, v76, v77
	v_cvt_pk_fp8_f32 v160, v83, v84 op_sel:[0,0,1]
	v_cvt_pk_fp8_f32 v161, v87, v88 op_sel:[0,0,1]
	v_cvt_pk_fp8_f32 v162, v91, v92 op_sel:[0,0,1]
	v_cvt_pk_fp8_f32 v163, v95, v96 op_sel:[0,0,1]
	v_cvt_pk_fp8_f32 v164, v66, v67 op_sel:[0,0,1]
	v_cvt_pk_fp8_f32 v165, v70, v71 op_sel:[0,0,1]
	v_cvt_pk_fp8_f32 v166, v74, v75 op_sel:[0,0,1]
	v_cvt_pk_fp8_f32 v167, v78, v79 op_sel:[0,0,1]
	s_lshl_b32 s6, s4, 7
	s_and_b32 s6, s6, 0xfffffc00
	v_mfma_scale_f32_16x16x128_f8f6f4 v[48:51], v[144:151], v[160:167], v[48:51], v194, v194 op_sel_hi:[0,0,0]
	s_nop 15
	s_nop 3
	s_lshl_b32 s4, s4, 6
	v_mul_f32_e32 v48, 0x41800000, v48
	s_waitcnt lgkmcnt(0)
	v_mfma_scale_f32_32x32x64_f8f6f4 v[32:47], v[128:135], v[160:167], v[32:47], v194, v194 op_sel_hi:[0,0,0]
	v_div_scale_f32 v49, s[30:31], v48, v48, s37
	v_rcp_f32_e32 v66, v49
	s_mov_b64 s[30:31], 0
	v_fma_f32 v50, -v49, v66, 1.0
	v_fmac_f32_e32 v66, v50, v66
	v_div_scale_f32 v50, vcc, s37, v48, s37
	v_mul_f32_e32 v51, v50, v66
	v_fma_f32 v52, -v49, v51, v50
	v_fmac_f32_e32 v51, v52, v66
	v_fma_f32 v49, -v49, v51, v50
	v_div_fmas_f32 v49, v49, v66, v51
	v_mfma_scale_f32_32x32x64_f8f6f4 v[16:31], v[136:143], v[160:167], v[16:31], v194, v194 op_sel_hi:[0,0,0]
	v_div_fixup_f32 v48, v49, v48, s37
	s_nop 6
	v_mul_f32_e32 v32, v48, v32
	v_mul_f32_e32 v33, v48, v33
	v_mov_b32_e32 v49, 0
	v_cvt_pk_fp8_f32 v49, v32, v33
	v_mul_f32_e32 v32, v48, v34
	v_mul_f32_e32 v33, v48, v35
	s_and_b64 vcc, exec, s[28:29]
	v_cvt_pk_fp8_f32 v49, v32, v33 op_sel:[0,0,1]
	v_mov_b32_e32 v32, 0
	v_mov_b32_e32 v33, 0
	s_nop 1
	v_mul_f32_e32 v16, v48, v16
	v_mul_f32_e32 v17, v48, v17
	v_cvt_pk_fp8_f32 v32, v16, v17
	v_mul_f32_e32 v16, v48, v36
	v_mul_f32_e32 v17, v48, v37
	v_cvt_pk_fp8_f32 v33, v16, v17
	v_mul_f32_e32 v18, v48, v18
	v_mul_f32_e32 v19, v48, v19
	v_mul_f32_e32 v16, v48, v38
	v_mul_f32_e32 v17, v48, v39
	v_cvt_pk_fp8_f32 v32, v18, v19 op_sel:[0,0,1]
	v_cvt_pk_fp8_f32 v33, v16, v17 op_sel:[0,0,1]
	v_mul_f32_e32 v16, v48, v20
	v_mul_f32_e32 v17, v48, v21
	v_mov_b32_e32 v18, 0
	v_cvt_pk_fp8_f32 v18, v16, v17
	v_mul_f32_e32 v17, v48, v22
	v_mul_f32_e32 v19, v48, v23
	v_mov_b32_e32 v22, 0
	v_cvt_pk_fp8_f32 v18, v17, v19 op_sel:[0,0,1]
	v_mul_f32_e32 v17, v48, v40
	v_mul_f32_e32 v19, v48, v41
	v_cvt_pk_fp8_f32 v22, v17, v19
	v_mul_f32_e32 v17, v48, v24
	v_mul_f32_e32 v19, v48, v25
	v_mov_b32_e32 v23, 0
	v_cvt_pk_fp8_f32 v23, v17, v19
	v_mul_f32_e32 v17, v48, v26
	v_mul_f32_e32 v19, v48, v27
	v_mov_b32_e32 v24, 0
	v_cvt_pk_fp8_f32 v23, v17, v19 op_sel:[0,0,1]
	v_mul_f32_e32 v17, v48, v44
	v_mul_f32_e32 v19, v48, v45
	v_cvt_pk_fp8_f32 v24, v17, v19
	v_mul_f32_e32 v17, v48, v28
	v_mul_f32_e32 v19, v48, v29
	v_mov_b32_e32 v25, 0
	v_cvt_pk_fp8_f32 v25, v17, v19
	v_mul_f32_e32 v20, v48, v42
	v_mul_f32_e32 v21, v48, v43
	v_cvt_pk_fp8_f32 v22, v20, v21 op_sel:[0,0,1]
	v_mul_f32_e32 v20, v48, v46
	v_mul_f32_e32 v21, v48, v47
	v_cvt_pk_fp8_f32 v24, v20, v21 op_sel:[0,0,1]
	v_mul_f32_e32 v17, v48, v30
	v_mul_f32_e32 v19, v48, v31
	v_add_u32_e32 v16, 0x10000, v196
	v_cvt_pk_fp8_f32 v25, v17, v19 op_sel:[0,0,1]
	ds_write2_b32 v16, v49, v33 offset1:2
	ds_write2_b32 v16, v32, v18 offset0:8 offset1:10
	ds_write2_b32 v16, v22, v24 offset0:4 offset1:6
	ds_write2_b32 v16, v23, v25 offset0:12 offset1:14
	v_add_u32_e32 v16, s6, v172
	v_ashrrev_i32_e32 v17, 31, v16
	s_waitcnt lgkmcnt(0)
	v_lshlrev_b64 v[16:17], 6, v[16:17]
	v_lshl_add_u64 v[20:21], s[12:13], 0, v[16:17]
	s_and_b32 s6, s4, 0x1c0
	s_lshl_b32 s6, s6, 14
	ds_read_b128 v[16:19], v197
	v_lshl_add_u64 v[24:25], v[20:21], 0, s[6:7]
	ds_read_b128 v[20:23], v198
	v_lshl_add_u64 v[24:25], v[24:25], 0, v[170:171]
	v_lshl_add_u64 v[26:27], v[24:25], 0, v[184:185]
	s_waitcnt lgkmcnt(0)
	global_store_dwordx4 v[26:27], v[16:19], off sc1
	s_mov_b32 s4, s34
	v_mov_b32_e32 v172, v80
	v_lshl_add_u64 v[16:17], v[24:25], 0, v[186:187]
	global_store_dwordx4 v[16:17], v[20:23], off sc1
	s_waitcnt lgkmcnt(0)
	s_cbranch_vccnz .LBB3_18

amdhsa.kernels:
  - .agpr_count:     0
    .args:
      - .actual_access:  read_only
        .address_space:  global
        .offset:         0
        .size:           8
        .value_kind:     global_buffer
      - .actual_access:  read_only
        .address_space:  global
        .offset:         8
        .size:           8
        .value_kind:     global_buffer
      - .actual_access:  read_only
        .address_space:  global
        .offset:         16
        .size:           8
        .value_kind:     global_buffer
      - .actual_access:  read_only
        .address_space:  global
        .offset:         24
        .size:           8
        .value_kind:     global_buffer
      - .actual_access:  read_only
        .address_space:  global
        .offset:         32
        .size:           8
        .value_kind:     global_buffer
      - .actual_access:  read_only
        .address_space:  global
        .offset:         40
        .size:           8
        .value_kind:     global_buffer
      - .actual_access:  read_only
        .address_space:  global
        .offset:         48
        .size:           8
        .value_kind:     global_buffer
      - .actual_access:  write_only
        .address_space:  global
        .offset:         56
        .size:           8
        .value_kind:     global_buffer
    .group_segment_fixed_size: 32
    .kernarg_segment_align: 8
    .kernarg_segment_size: 64
    .language:       OpenCL C
    .language_version:
      - 2
      - 0
    .max_flat_workgroup_size: 256
    .name:           _Z11prep_kernelPKfS0_S0_S0_S0_S0_S0_Pc
    .private_segment_fixed_size: 0
    .sgpr_count:     48
    .sgpr_spill_count: 0
    .symbol:         _Z11prep_kernelPKfS0_S0_S0_S0_S0_S0_Pc.kd
    .uniform_work_group_size: 1
    .uses_dynamic_stack: false
    .vgpr_count:     78
    .vgpr_spill_count: 0
    .wavefront_size: 64
  - .agpr_count:     0
    .args:
      - .address_space:  global
        .offset:         0
        .size:           8
        .value_kind:     global_buffer
      - .actual_access:  read_only
        .address_space:  global
        .offset:         8
        .size:           8
        .value_kind:     global_buffer
      - .actual_access:  read_only
        .address_space:  global
        .offset:         16
        .size:           8
        .value_kind:     global_buffer
    .group_segment_fixed_size: 0
    .kernarg_segment_align: 8
    .kernarg_segment_size: 24
    .language:       OpenCL C
    .language_version:
      - 2
      - 0
    .max_flat_workgroup_size: 512
    .name:           _Z13qkv256_kernelPcPKfS1_
    .private_segment_fixed_size: 0
    .sgpr_count:     35
    .sgpr_spill_count: 0
    .symbol:         _Z13qkv256_kernelPcPKfS1_.kd
    .uniform_work_group_size: 1
    .uses_dynamic_stack: false
    .vgpr_count:     214
    .vgpr_spill_count: 0
    .wavefront_size: 64
  - .agpr_count:     0
    .args:
      - .address_space:  global
        .offset:         0
        .size:           8
        .value_kind:     global_buffer
      - .actual_access:  read_only
        .address_space:  global
        .offset:         8
        .size:           8
        .value_kind:     global_buffer
      - .actual_access:  read_only
        .address_space:  global
        .offset:         16
        .size:           8
        .value_kind:     global_buffer
      - .actual_access:  write_only
        .address_space:  global
        .offset:         24
        .size:           8
        .value_kind:     global_buffer
    .group_segment_fixed_size: 0
    .kernarg_segment_align: 8
    .kernarg_segment_size: 32
    .language:       OpenCL C
    .language_version:
      - 2
      - 0
    .max_flat_workgroup_size: 256
    .name:           _Z11proj_kernelPKcPKfS2_Pf
    .private_segment_fixed_size: 0
    .sgpr_count:     34
    .sgpr_spill_count: 0
    .symbol:         _Z11proj_kernelPKcPKfS2_Pf.kd
    .uniform_work_group_size: 1
    .uses_dynamic_stack: false
    .vgpr_count:     196
    .vgpr_spill_count: 0
    .wavefront_size: 64
  - .agpr_count:     0
    .args:
      - .address_space:  global
        .offset:         0
        .size:           8
        .value_kind:     global_buffer
      - .offset:         8
        .size:           4
        .value_kind:     hidden_block_count_x
      - .offset:         12
        .size:           4
        .value_kind:     hidden_block_count_y
      - .offset:         16
        .size:           4
        .value_kind:     hidden_block_count_z
      - .offset:         20
        .size:           2
        .value_kind:     hidden_group_size_x
      - .offset:         22
        .size:           2
        .value_kind:     hidden_group_size_y
      - .offset:         24
        .size:           2
        .value_kind:     hidden_group_size_z
      - .offset:         26
        .size:           2
        .value_kind:     hidden_remainder_x
      - .offset:         28
        .size:           2
        .value_kind:     hidden_remainder_y
      - .offset:         30
        .size:           2
        .value_kind:     hidden_remainder_z
      - .offset:         48
        .size:           8
        .value_kind:     hidden_global_offset_x
      - .offset:         56
        .size:           8
        .value_kind:     hidden_global_offset_y
      - .offset:         64
        .size:           8
        .value_kind:     hidden_global_offset_z
      - .offset:         72
        .size:           2
        .value_kind:     hidden_grid_dims
      - .offset:         128
        .size:           4
        .value_kind:     hidden_dynamic_lds_size
    .group_segment_fixed_size: 16384
    .kernarg_segment_align: 8
    .kernarg_segment_size: 264
    .language:       OpenCL C
    .language_version:
      - 2
      - 0
    .max_flat_workgroup_size: 256
    .name:           _Z13attn11_kernelILi4EEvPc
    .private_segment_fixed_size: 0
    .sgpr_count:     74
    .sgpr_spill_count: 0
    .symbol:         _Z13attn11_kernelILi4EEvPc.kd
    .uniform_work_group_size: 1
    .uses_dynamic_stack: false
    .vgpr_count:     230
    .vgpr_spill_count: 0
    .wavefront_size: 64
